# speedup vs baseline: 1.0303x; 1.0031x over previous
.Lmy_back_3:
	v_add_f32_e32 v197, v187, v48
	s_nop 7
	s_nop 3

.LBB2_18:
	s_waitcnt vmcnt(0) lgkmcnt(0)
	s_barrier
	v_add_f32_e32 v198, v80, v81
	v_add_f32_e32 v198, v82, v198
	v_add_f32_e32 v198, v83, v198
	v_add_f32_e32 v198, v84, v198
	v_add_f32_e32 v198, v85, v198
	v_add_f32_e32 v198, v86, v198
	v_add_f32_e32 v198, v87, v198
	v_add_f32_e32 v198, v88, v198
	v_add_f32_e32 v198, v89, v198
	v_add_f32_e32 v198, v90, v198
	v_add_f32_e32 v198, v91, v198
	v_add_f32_e32 v198, v92, v198
	v_add_f32_e32 v198, v93, v198
	v_add_f32_e32 v198, v94, v198
	v_add_f32_e32 v198, v95, v198
	v_add_f32_e32 v198, v0, v198
	v_add_f32_e32 v198, v1, v198
	v_add_f32_e32 v198, v2, v198
	v_add_f32_e32 v198, v3, v198
	v_add_f32_e32 v198, v4, v198
	v_add_f32_e32 v198, v5, v198
	v_add_f32_e32 v198, v6, v198
	v_add_f32_e32 v198, v7, v198
	v_add_f32_e32 v198, v8, v198
	v_add_f32_e32 v198, v9, v198
	v_add_f32_e32 v198, v10, v198
	v_add_f32_e32 v198, v11, v198
	v_add_f32_e32 v198, v12, v198
	v_add_f32_e32 v198, v13, v198
	v_add_f32_e32 v198, v14, v198
	v_add_f32_e32 v198, v15, v198
	v_cmp_lt_f32_e32 vcc, s36, v198
	s_nop 4
	s_cbranch_vccnz .Lmy_rare_4
.Lmy_back_4:
	ds_read_b64_tr_b16 v[54:55], v192 offset:49152
	ds_read_b64_tr_b16 v[56:57], v192 offset:49664
	v_add_f32_e32 v49, v80, v81
	v_cvt_pk_f16_f32 v50, v80, v81
	v_cvt_pk_f16_f32 v51, v82, v83
	v_cvt_pk_f16_f32 v52, v84, v85
	v_cvt_pk_f16_f32 v53, v86, v87
	ds_read_b64_tr_b16 v[58:59], v192 offset:50176
	ds_read_b64_tr_b16 v[60:61], v192 offset:50688
	s_waitcnt lgkmcnt(2)
	v_mfma_f32_32x32x16_f16 v[16:31], v[50:53], v[54:57], v[16:31]
	ds_read_b64_tr_b16 v[54:55], v192 offset:53248
	ds_read_b64_tr_b16 v[56:57], v192 offset:53760
	v_add_f32_e32 v49, v82, v49
	v_add_f32_e32 v49, v83, v49
	v_add_f32_e32 v49, v84, v49
	v_add_f32_e32 v49, v85, v49
	v_add_f32_e32 v49, v86, v49
	v_add_f32_e32 v49, v87, v49
	s_waitcnt lgkmcnt(0)
	v_mfma_f32_32x32x16_f16 v[32:47], v[50:53], v[54:57], v[32:47]
	v_add_f32_e32 v49, v88, v49
	v_add_f32_e32 v49, v89, v49
	ds_read_b64_tr_b16 v[62:63], v192 offset:54272
	ds_read_b64_tr_b16 v[64:65], v192 offset:54784
	v_add_f32_e32 v49, v90, v49
	v_add_f32_e32 v49, v91, v49
	v_cvt_pk_f16_f32 v50, v88, v89
	v_cvt_pk_f16_f32 v51, v90, v91
	v_cvt_pk_f16_f32 v52, v92, v93
	v_cvt_pk_f16_f32 v53, v94, v95
	v_add_f32_e32 v49, v92, v49
	v_mfma_f32_32x32x16_f16 v[16:31], v[50:53], v[58:61], v[16:31]
	v_add_f32_e32 v49, v93, v49
	v_add_f32_e32 v49, v94, v49
	v_add_f32_e32 v49, v95, v49
	v_add_f32_e32 v49, v0, v49
	v_add_f32_e32 v49, v1, v49
	v_add_f32_e32 v49, v2, v49
	v_add_f32_e32 v49, v3, v49
	s_waitcnt lgkmcnt(0)
	v_mfma_f32_32x32x16_f16 v[32:47], v[50:53], v[62:65], v[32:47]
	ds_read_b64_tr_b16 v[50:51], v192 offset:51200
	ds_read_b64_tr_b16 v[52:53], v192 offset:51712
	v_cvt_pk_f16_f32 v0, v0, v1
	v_cvt_pk_f16_f32 v1, v2, v3
	v_cvt_pk_f16_f32 v2, v4, v5
	v_cvt_pk_f16_f32 v3, v6, v7
	ds_read_b64_tr_b16 v[54:55], v192 offset:52224
	ds_read_b64_tr_b16 v[56:57], v192 offset:52736
	v_add_f32_e32 v4, v4, v49
	s_waitcnt lgkmcnt(2)
	v_mfma_f32_32x32x16_f16 v[16:31], v[0:3], v[50:53], v[16:31]
	ds_read_b64_tr_b16 v[50:51], v192 offset:55296
	ds_read_b64_tr_b16 v[52:53], v192 offset:55808
	v_add_f32_e32 v4, v5, v4
	v_add_f32_e32 v4, v6, v4
	ds_read_b64_tr_b16 v[58:59], v192 offset:56320
	ds_read_b64_tr_b16 v[60:61], v192 offset:56832
	v_cvt_pk_f16_f32 v5, v14, v15
	s_waitcnt lgkmcnt(2)
	v_mfma_f32_32x32x16_f16 v[32:47], v[0:3], v[50:53], v[32:47]
	v_add_f32_e32 v0, v7, v4
	v_add_f32_e32 v0, v8, v0
	v_add_f32_e32 v0, v9, v0
	v_add_f32_e32 v0, v10, v0
	v_cvt_pk_f16_f32 v2, v8, v9
	v_cvt_pk_f16_f32 v3, v10, v11
	v_cvt_pk_f16_f32 v4, v12, v13
	v_add_f32_e32 v0, v11, v0
	v_mfma_f32_32x32x16_f16 v[16:31], v[2:5], v[54:57], v[16:31]
	v_add_f32_e32 v0, v12, v0
	v_add_f32_e32 v0, v13, v0
	v_add_f32_e32 v0, v14, v0
	v_add_f32_e32 v0, v15, v0
	v_add_f32_e32 v0, v197, v0
	v_mov_b32_e32 v1, v0
	s_nop 1
	v_permlane32_swap_b32_e32 v0, v1
	s_waitcnt lgkmcnt(0)
	v_mfma_f32_32x32x16_f16 v[32:47], v[2:5], v[58:61], v[32:47]
	s_and_saveexec_b64 s[2:3], s[0:1]
	v_add_f32_e32 v0, v0, v1
	ds_write_b32 v186, v0 offset:57472
	s_or_b64 exec, exec, s[2:3]
	s_waitcnt lgkmcnt(0)
	ds_read_b128 v[0:3], v48 offset:57472
	ds_read_b128 v[4:7], v48 offset:57504
	s_mov_b32 s11, 0
	s_lshl_b64 s[0:1], s[10:11], 22
	s_add_u32 s0, s8, s0
	s_waitcnt lgkmcnt(1)
	v_rcp_f32_e32 v8, v0
	v_rcp_f32_e32 v9, v1
	s_addc_u32 s1, s9, s1
	s_lshl_b32 s2, s23, 12
	v_rcp_f32_e32 v10, v2
	v_rcp_f32_e32 v11, v3
	s_waitcnt lgkmcnt(0)
	v_rcp_f32_e32 v12, v4
	ds_read_b128 v[0:3], v48 offset:57536
	v_rcp_f32_e32 v13, v5
	v_rcp_f32_e32 v14, v6
	v_rcp_f32_e32 v15, v7
	ds_read_b128 v[4:7], v48 offset:57568
	s_add_i32 s6, s2, 0
	v_lshlrev_b32_e32 v48, 1, v189
	v_add3_u32 v48, s6, v191, v48
	v_fma_mixlo_f16 v16, v16, v8, 0
	v_fma_mixlo_f16 v8, v32, v8, 0
	ds_write_b16 v48, v8 offset:59456
	v_fma_mixlo_f16 v8, v17, v9, 0
	ds_write_b16 v48, v8 offset:59520
	v_fma_mixlo_f16 v8, v33, v9, 0
	ds_write_b16 v48, v8 offset:59584
	v_fma_mixlo_f16 v8, v18, v10, 0
	ds_write_b16 v48, v8 offset:59648
	v_fma_mixlo_f16 v8, v34, v10, 0
	ds_write_b16 v48, v8 offset:59712
	v_fma_mixlo_f16 v8, v19, v11, 0
	ds_write_b16 v48, v8 offset:59776
	v_fma_mixlo_f16 v8, v35, v11, 0
	ds_write_b16 v48, v8 offset:59840
	v_fma_mixlo_f16 v8, v20, v12, 0
	ds_write_b16 v48, v8 offset:60416
	v_fma_mixlo_f16 v8, v36, v12, 0
	ds_write_b16 v48, v8 offset:60480
	v_fma_mixlo_f16 v8, v21, v13, 0
	ds_write_b16 v48, v8 offset:60544
	v_fma_mixlo_f16 v8, v37, v13, 0
	s_waitcnt lgkmcnt(11)
	v_rcp_f32_e32 v0, v0
	ds_write_b16 v48, v8 offset:60608
	v_fma_mixlo_f16 v8, v22, v14, 0
	v_rcp_f32_e32 v1, v1
	ds_write_b16 v48, v8 offset:60672
	v_fma_mixlo_f16 v8, v38, v14, 0
	ds_write_b16 v48, v8 offset:60736
	v_fma_mixlo_f16 v8, v23, v15, 0
	v_rcp_f32_e32 v2, v2
	ds_write_b16 v48, v8 offset:60800
	v_fma_mixlo_f16 v8, v39, v15, 0
	ds_write_b16 v48, v8 offset:60864
	v_fma_mixlo_f16 v8, v24, v0, 0
	v_fma_mixlo_f16 v0, v40, v0, 0
	v_rcp_f32_e32 v3, v3
	ds_write_b16 v48, v0 offset:61504
	v_fma_mixlo_f16 v0, v25, v1, 0
	ds_write_b16 v48, v0 offset:61568
	v_fma_mixlo_f16 v0, v41, v1, 0
	s_waitcnt lgkmcnt(14)
	v_rcp_f32_e32 v4, v4
	ds_write_b16 v48, v0 offset:61632
	v_fma_mixlo_f16 v0, v26, v2, 0
	ds_write_b16 v48, v0 offset:61696
	v_fma_mixlo_f16 v0, v42, v2, 0
	v_rcp_f32_e32 v5, v5
	ds_write_b16 v48, v0 offset:61760
	v_fma_mixlo_f16 v0, v27, v3, 0
	ds_write_b16 v48, v0 offset:61824
	v_fma_mixlo_f16 v0, v43, v3, 0
	v_rcp_f32_e32 v6, v6
	ds_write_b16 v48, v0 offset:61888
	v_fma_mixlo_f16 v0, v28, v4, 0
	ds_write_b16 v48, v0 offset:62464
	v_fma_mixlo_f16 v0, v44, v4, 0
	v_rcp_f32_e32 v7, v7
	ds_write_b16 v48, v0 offset:62528
	v_fma_mixlo_f16 v0, v29, v5, 0
	ds_write_b16 v48, v0 offset:62592
	v_fma_mixlo_f16 v0, v45, v5, 0
	ds_write_b16 v48, v0 offset:62656
	v_fma_mixlo_f16 v0, v30, v6, 0
	ds_write_b16 v48, v0 offset:62720
	v_fma_mixlo_f16 v0, v46, v6, 0
	ds_write_b16 v48, v0 offset:62784
	v_fma_mixlo_f16 v0, v31, v7, 0
	ds_write_b16 v48, v0 offset:62848
	v_fma_mixlo_f16 v0, v47, v7, 0
	ds_write_b16 v48, v0 offset:62912
	v_lshrrev_b32_e32 v0, 3, v188
	v_and_b32_e32 v4, 56, v190
	s_lshl_b32 s4, s24, 8
	s_lshl_b32 s5, s22, 9
	ds_write_b16 v48, v16 offset:59392
	ds_write_b16 v48, v8 offset:61440
	v_lshlrev_b32_e32 v1, 7, v0
	v_lshlrev_b32_e32 v2, 1, v4
	s_waitcnt lgkmcnt(0)
	v_add3_u32 v8, s6, v1, v2
	s_or_b32 s4, s4, s5
	v_or_b32_e32 v5, s4, v0
	ds_read_b128 v[0:3], v8 offset:59392
	s_lshl_b32 s7, s20, 6
	v_add_lshl_u32 v5, v5, s21, 8
	v_or3_b32 v4, v5, s7, v4
	s_and_b32 s1, s1, 0xffff
	s_mov_b32 s3, 0x20000
	s_mov_b32 s2, 0x400000
	v_lshlrev_b32_e32 v12, 1, v4
	ds_read_b128 v[4:7], v8 offset:60416
	s_waitcnt lgkmcnt(1)
	buffer_store_dwordx4 v[0:3], v12, s[0:3], 0 offen sc1
	ds_read_b128 v[0:3], v8 offset:61440
	ds_read_b128 v[8:11], v8 offset:62464
	v_add_u32_e32 v13, 0x1000, v12
	s_waitcnt lgkmcnt(2)
	buffer_store_dwordx4 v[4:7], v13, s[0:3], 0 offen sc1
	s_nop 1
	v_add_u32_e32 v4, 0x2000, v12
	s_waitcnt lgkmcnt(1)
	buffer_store_dwordx4 v[0:3], v4, s[0:3], 0 offen sc1
	s_nop 1
	v_add_u32_e32 v0, 0x3000, v12
	s_waitcnt lgkmcnt(0)
	buffer_store_dwordx4 v[8:11], v0, s[0:3], 0 offen sc1
	s_waitcnt lgkmcnt(0)
	s_barrier
	s_endpgm
.Lmy_rare_1:
	v_subrev_u32_e32 v160, s25, v191
	v_add_u32_e32 v160, 0xffffe000, v160
	v_ashrrev_i32_e32 v161, 31, v160
	v_lshl_add_u64 v[160:161], v[182:183], 0, v[160:161]
	s_mov_b64 s[38:39], 0x1000
	v_lshl_add_u64 v[162:163], v[160:161], 0, s[38:39]
	v_xor_b32_e32 v166, 0x80000000, v194
	s_lshl_b32 s42, s23, 12
	v_lshlrev_b32_e32 v167, 2, v188
	v_add_u32_e32 v167, s42, v167
	global_load_dwordx4 v[140:143], v[160:161], off
	global_load_dwordx4 v[132:135], v[160:161], off offset:2048
	global_load_dwordx4 v[124:127], v[162:163], off
	global_load_dwordx4 v[116:119], v[162:163], off offset:2048
	v_mov_b32_e32 v144, v166
	v_mov_b32_e32 v145, v166
	v_mov_b32_e32 v146, v166
	v_mov_b32_e32 v147, v166
	v_mov_b32_e32 v148, v166
	v_mov_b32_e32 v149, v166
	v_mov_b32_e32 v150, v166
	v_mov_b32_e32 v151, v166
	v_mov_b32_e32 v152, v166
	v_mov_b32_e32 v153, v166
	v_mov_b32_e32 v154, v166
	v_mov_b32_e32 v155, v166
	v_mov_b32_e32 v156, v166
	v_mov_b32_e32 v157, v166
	v_mov_b32_e32 v158, v166
	v_mov_b32_e32 v159, v166
	s_waitcnt vmcnt(0)
	v_mfma_f32_32x32x16_f16 v[144:159], v[140:143], v[136:139], v[144:159]
	v_mfma_f32_32x32x16_f16 v[144:159], v[132:135], v[128:131], v[144:159]
	v_mfma_f32_32x32x16_f16 v[144:159], v[124:127], v[120:123], v[144:159]
	v_mfma_f32_32x32x16_f16 v[144:159], v[116:119], v[112:115], v[144:159]
	s_nop 15
	s_nop 3
	v_max3_f32 v164, v144, v145, v146
	v_max3_f32 v164, v164, v147, v148
	v_max3_f32 v164, v164, v149, v150
	v_max3_f32 v164, v164, v151, v152
	v_max3_f32 v164, v164, v153, v154
	v_max3_f32 v164, v164, v155, v156
	v_max3_f32 v164, v164, v157, v158
	v_max_f32_e32 v164, v164, v159
	ds_write_b32 v167, v144 offset:59392
	ds_write_b32 v167, v145 offset:59648
	ds_write_b32 v167, v146 offset:59904
	ds_write_b32 v167, v147 offset:60160
	ds_write_b32 v167, v148 offset:60416
	ds_write_b32 v167, v149 offset:60672
	ds_write_b32 v167, v150 offset:60928
	ds_write_b32 v167, v151 offset:61184
	ds_write_b32 v167, v152 offset:61440
	ds_write_b32 v167, v153 offset:61696
	ds_write_b32 v167, v154 offset:61952
	ds_write_b32 v167, v155 offset:62208
	ds_write_b32 v167, v156 offset:62464
	ds_write_b32 v167, v157 offset:62720
	ds_write_b32 v167, v158 offset:62976
	ds_write_b32 v167, v159 offset:63232
	s_waitcnt lgkmcnt(0)
	global_load_dwordx4 v[140:143], v[160:161], off offset:512
	global_load_dwordx4 v[132:135], v[160:161], off offset:2560
	global_load_dwordx4 v[124:127], v[162:163], off offset:512
	global_load_dwordx4 v[116:119], v[162:163], off offset:2560
	v_mov_b32_e32 v144, v166
	v_mov_b32_e32 v145, v166
	v_mov_b32_e32 v146, v166
	v_mov_b32_e32 v147, v166
	v_mov_b32_e32 v148, v166
	v_mov_b32_e32 v149, v166
	v_mov_b32_e32 v150, v166
	v_mov_b32_e32 v151, v166
	v_mov_b32_e32 v152, v166
	v_mov_b32_e32 v153, v166
	v_mov_b32_e32 v154, v166
	v_mov_b32_e32 v155, v166
	v_mov_b32_e32 v156, v166
	v_mov_b32_e32 v157, v166
	v_mov_b32_e32 v158, v166
	v_mov_b32_e32 v159, v166
	s_waitcnt vmcnt(0)
	v_mfma_f32_32x32x16_f16 v[144:159], v[140:143], v[136:139], v[144:159]
	v_mfma_f32_32x32x16_f16 v[144:159], v[132:135], v[128:131], v[144:159]
	v_mfma_f32_32x32x16_f16 v[144:159], v[124:127], v[120:123], v[144:159]
	v_mfma_f32_32x32x16_f16 v[144:159], v[116:119], v[112:115], v[144:159]
	s_nop 15
	s_nop 3
	v_max3_f32 v165, v144, v145, v146
	v_max3_f32 v165, v165, v147, v148
	v_max3_f32 v165, v165, v149, v150
	v_max3_f32 v165, v165, v151, v152
	v_max3_f32 v165, v165, v153, v154
	v_max3_f32 v165, v165, v155, v156
	v_max3_f32 v165, v165, v157, v158
	v_max_f32_e32 v165, v165, v159
	v_max_f32_e32 v164, v164, v165
	v_mov_b32_e32 v165, v164
	s_nop 1
	v_permlane32_swap_b32_e32 v164, v165
	v_max_f32_e32 v164, v165, v164
	s_mov_b32 s37, 0x41000000
	v_cmp_lt_f32_e32 vcc, s37, v164
	v_max_f32_e32 v164, 0, v164
	s_nop 4
	s_cbranch_vccnz .Lmy_rare_1_rs
	v_mov_b32_e32 v164, 0
	s_branch .Lmy_rare_1_nr
.Lmy_rare_1_rs:
	v_add_f32_e32 v194, v194, v164
	v_exp_f32_e64 v165, -v164
	v_sub_f32_e32 v96, v96, v164
	v_sub_f32_e32 v97, v97, v164
	v_sub_f32_e32 v98, v98, v164
	v_sub_f32_e32 v99, v99, v164
	v_sub_f32_e32 v100, v100, v164
	v_sub_f32_e32 v101, v101, v164
	v_sub_f32_e32 v102, v102, v164
	v_sub_f32_e32 v103, v103, v164
	v_sub_f32_e32 v104, v104, v164
	v_sub_f32_e32 v105, v105, v164
	v_sub_f32_e32 v106, v106, v164
	v_sub_f32_e32 v107, v107, v164
	v_sub_f32_e32 v108, v108, v164
	v_sub_f32_e32 v109, v109, v164
	v_sub_f32_e32 v110, v110, v164
	v_sub_f32_e32 v111, v111, v164
	v_sub_f32_e32 v80, v80, v164
	v_sub_f32_e32 v81, v81, v164
	v_sub_f32_e32 v82, v82, v164
	v_sub_f32_e32 v83, v83, v164
	v_sub_f32_e32 v84, v84, v164
	v_sub_f32_e32 v85, v85, v164
	v_sub_f32_e32 v86, v86, v164
	v_sub_f32_e32 v87, v87, v164
	v_sub_f32_e32 v88, v88, v164
	v_sub_f32_e32 v89, v89, v164
	v_sub_f32_e32 v90, v90, v164
	v_sub_f32_e32 v91, v91, v164
	v_sub_f32_e32 v92, v92, v164
	v_sub_f32_e32 v93, v93, v164
	v_sub_f32_e32 v94, v94, v164
	v_sub_f32_e32 v95, v95, v164
	v_xor_b32_e32 v0, 0x80000000, v194
	v_mov_b32_e32 v1, v0
	v_mov_b32_e32 v2, v0
	v_mov_b32_e32 v3, v0
	v_mov_b32_e32 v4, v0
	v_mov_b32_e32 v5, v0
	v_mov_b32_e32 v6, v0
	v_mov_b32_e32 v7, v0
	v_mov_b32_e32 v8, v0
	v_mov_b32_e32 v9, v0
	v_mov_b32_e32 v10, v0
	v_mov_b32_e32 v11, v0
	v_mov_b32_e32 v12, v0
	v_mov_b32_e32 v13, v0
	v_mov_b32_e32 v14, v0
	v_mov_b32_e32 v15, v0
	v_mul_f32_e32 v187, v187, v165
	s_and_saveexec_b64 s[40:41], s[0:1]
	ds_write_b32 v186, v165 offset:57344
	s_or_b64 exec, exec, s[40:41]
	v_add_u32_e32 v166, s11, v193
	s_waitcnt lgkmcnt(0)
	ds_read_b128 v[140:143], v166 offset:57344
	ds_read_b128 v[132:135], v166 offset:57376
	ds_read_b128 v[124:127], v166 offset:57408
	ds_read_b128 v[116:119], v166 offset:57440
	s_waitcnt lgkmcnt(0)
	v_pk_mul_f32 v[16:17], v[16:17], v[140:141]
	v_pk_mul_f32 v[32:33], v[32:33], v[140:141]
	v_pk_mul_f32 v[18:19], v[18:19], v[142:143]
	v_pk_mul_f32 v[34:35], v[34:35], v[142:143]
	v_pk_mul_f32 v[20:21], v[20:21], v[132:133]
	v_pk_mul_f32 v[36:37], v[36:37], v[132:133]
	v_pk_mul_f32 v[22:23], v[22:23], v[134:135]
	v_pk_mul_f32 v[38:39], v[38:39], v[134:135]
	v_pk_mul_f32 v[24:25], v[24:25], v[124:125]
	v_pk_mul_f32 v[40:41], v[40:41], v[124:125]
	v_pk_mul_f32 v[26:27], v[26:27], v[126:127]
	v_pk_mul_f32 v[42:43], v[42:43], v[126:127]
	v_pk_mul_f32 v[28:29], v[28:29], v[116:117]
	v_pk_mul_f32 v[44:45], v[44:45], v[116:117]
	v_pk_mul_f32 v[30:31], v[30:31], v[118:119]
	v_pk_mul_f32 v[46:47], v[46:47], v[118:119]
.Lmy_rare_1_nr:
	v_sub_f32_e32 v144, v144, v164
	v_sub_f32_e32 v145, v145, v164
	v_sub_f32_e32 v146, v146, v164
	v_sub_f32_e32 v147, v147, v164
	v_sub_f32_e32 v148, v148, v164
	v_sub_f32_e32 v149, v149, v164
	v_sub_f32_e32 v150, v150, v164
	v_sub_f32_e32 v151, v151, v164
	v_sub_f32_e32 v152, v152, v164
	v_sub_f32_e32 v153, v153, v164
	v_sub_f32_e32 v154, v154, v164
	v_sub_f32_e32 v155, v155, v164
	v_sub_f32_e32 v156, v156, v164
	v_sub_f32_e32 v157, v157, v164
	v_sub_f32_e32 v158, v158, v164
	v_sub_f32_e32 v159, v159, v164
	v_exp_f32_e32 v144, v144
	v_exp_f32_e32 v145, v145
	v_exp_f32_e32 v146, v146
	v_exp_f32_e32 v147, v147
	v_exp_f32_e32 v148, v148
	v_exp_f32_e32 v149, v149
	v_exp_f32_e32 v150, v150
	v_exp_f32_e32 v151, v151
	v_exp_f32_e32 v152, v152
	v_exp_f32_e32 v153, v153
	v_exp_f32_e32 v154, v154
	v_exp_f32_e32 v155, v155
	v_exp_f32_e32 v156, v156
	v_exp_f32_e32 v157, v157
	v_exp_f32_e32 v158, v158
	v_exp_f32_e32 v159, v159
	s_nop 0
	v_add_f32_e32 v76, v144, v145
	v_add_f32_e32 v76, v146, v76
	v_add_f32_e32 v76, v147, v76
	v_add_f32_e32 v76, v148, v76
	v_add_f32_e32 v76, v149, v76
	v_add_f32_e32 v76, v150, v76
	v_add_f32_e32 v76, v151, v76
	v_add_f32_e32 v76, v152, v76
	v_add_f32_e32 v76, v153, v76
	v_add_f32_e32 v76, v154, v76
	v_add_f32_e32 v76, v155, v76
	v_add_f32_e32 v76, v156, v76
	v_add_f32_e32 v76, v157, v76
	v_add_f32_e32 v76, v158, v76
	v_add_f32_e32 v76, v159, v76
	v_cvt_pk_f16_f32 v124, v144, v145
	v_cvt_pk_f16_f32 v125, v146, v147
	v_cvt_pk_f16_f32 v126, v148, v149
	v_cvt_pk_f16_f32 v127, v150, v151
	v_cvt_pk_f16_f32 v116, v152, v153
	v_cvt_pk_f16_f32 v117, v154, v155
	v_cvt_pk_f16_f32 v118, v156, v157
	v_cvt_pk_f16_f32 v119, v158, v159
	ds_read_b32 v144, v167 offset:59392
	ds_read_b32 v145, v167 offset:59648
	ds_read_b32 v146, v167 offset:59904
	ds_read_b32 v147, v167 offset:60160
	ds_read_b32 v148, v167 offset:60416
	ds_read_b32 v149, v167 offset:60672
	ds_read_b32 v150, v167 offset:60928
	ds_read_b32 v151, v167 offset:61184
	ds_read_b32 v152, v167 offset:61440
	ds_read_b32 v153, v167 offset:61696
	ds_read_b32 v154, v167 offset:61952
	ds_read_b32 v155, v167 offset:62208
	ds_read_b32 v156, v167 offset:62464
	ds_read_b32 v157, v167 offset:62720
	ds_read_b32 v158, v167 offset:62976
	ds_read_b32 v159, v167 offset:63232
	s_waitcnt lgkmcnt(0)
	v_sub_f32_e32 v144, v144, v164
	v_sub_f32_e32 v145, v145, v164
	v_sub_f32_e32 v146, v146, v164
	v_sub_f32_e32 v147, v147, v164
	v_sub_f32_e32 v148, v148, v164
	v_sub_f32_e32 v149, v149, v164
	v_sub_f32_e32 v150, v150, v164
	v_sub_f32_e32 v151, v151, v164
	v_sub_f32_e32 v152, v152, v164
	v_sub_f32_e32 v153, v153, v164
	v_sub_f32_e32 v154, v154, v164
	v_sub_f32_e32 v155, v155, v164
	v_sub_f32_e32 v156, v156, v164
	v_sub_f32_e32 v157, v157, v164
	v_sub_f32_e32 v158, v158, v164
	v_sub_f32_e32 v159, v159, v164
	v_exp_f32_e32 v144, v144
	v_exp_f32_e32 v145, v145
	v_exp_f32_e32 v146, v146
	v_exp_f32_e32 v147, v147
	v_exp_f32_e32 v148, v148
	v_exp_f32_e32 v149, v149
	v_exp_f32_e32 v150, v150
	v_exp_f32_e32 v151, v151
	v_exp_f32_e32 v152, v152
	v_exp_f32_e32 v153, v153
	v_exp_f32_e32 v154, v154
	v_exp_f32_e32 v155, v155
	v_exp_f32_e32 v156, v156
	v_exp_f32_e32 v157, v157
	v_exp_f32_e32 v158, v158
	v_exp_f32_e32 v159, v159
	s_nop 0
	v_add_f32_e32 v76, v144, v76
	v_add_f32_e32 v76, v145, v76
	v_add_f32_e32 v76, v146, v76
	v_add_f32_e32 v76, v147, v76
	v_add_f32_e32 v76, v148, v76
	v_add_f32_e32 v76, v149, v76
	v_add_f32_e32 v76, v150, v76
	v_add_f32_e32 v76, v151, v76
	v_add_f32_e32 v76, v152, v76
	v_add_f32_e32 v76, v153, v76
	v_add_f32_e32 v76, v154, v76
	v_add_f32_e32 v76, v155, v76
	v_add_f32_e32 v76, v156, v76
	v_add_f32_e32 v76, v157, v76
	v_add_f32_e32 v76, v158, v76
	v_add_f32_e32 v76, v159, v76
	v_cvt_pk_f16_f32 v140, v144, v145
	v_cvt_pk_f16_f32 v141, v146, v147
	v_cvt_pk_f16_f32 v142, v148, v149
	v_cvt_pk_f16_f32 v143, v150, v151
	v_cvt_pk_f16_f32 v132, v152, v153
	v_cvt_pk_f16_f32 v133, v154, v155
	v_cvt_pk_f16_f32 v134, v156, v157
	v_cvt_pk_f16_f32 v135, v158, v159
	s_branch .Lmy_back_1
.Lmy_rare_2:
	v_subrev_u32_e32 v172, s25, v191
	v_ashrrev_i32_e32 v173, 31, v172
	v_lshl_add_u64 v[172:173], v[182:183], 0, v[172:173]
	s_mov_b64 s[38:39], 0x1000
	v_lshl_add_u64 v[174:175], v[172:173], 0, s[38:39]
	v_xor_b32_e32 v178, 0x80000000, v194
	s_lshl_b32 s42, s23, 12
	v_lshlrev_b32_e32 v179, 2, v188
	v_add_u32_e32 v179, s42, v179
	global_load_dwordx4 v[140:143], v[172:173], off
	global_load_dwordx4 v[132:135], v[172:173], off offset:2048
	global_load_dwordx4 v[124:127], v[174:175], off
	global_load_dwordx4 v[116:119], v[174:175], off offset:2048
	v_mov_b32_e32 v156, v178
	v_mov_b32_e32 v157, v178
	v_mov_b32_e32 v158, v178
	v_mov_b32_e32 v159, v178
	v_mov_b32_e32 v160, v178
	v_mov_b32_e32 v161, v178
	v_mov_b32_e32 v162, v178
	v_mov_b32_e32 v163, v178
	v_mov_b32_e32 v164, v178
	v_mov_b32_e32 v165, v178
	v_mov_b32_e32 v166, v178
	v_mov_b32_e32 v167, v178
	v_mov_b32_e32 v168, v178
	v_mov_b32_e32 v169, v178
	v_mov_b32_e32 v170, v178
	v_mov_b32_e32 v171, v178
	s_waitcnt vmcnt(0)
	v_mfma_f32_32x32x16_f16 v[156:171], v[140:143], v[136:139], v[156:171]
	v_mfma_f32_32x32x16_f16 v[156:171], v[132:135], v[128:131], v[156:171]
	v_mfma_f32_32x32x16_f16 v[156:171], v[124:127], v[120:123], v[156:171]
	v_mfma_f32_32x32x16_f16 v[156:171], v[116:119], v[112:115], v[156:171]
	s_nop 15
	s_nop 3
	v_max3_f32 v176, v156, v157, v158
	v_max3_f32 v176, v176, v159, v160
	v_max3_f32 v176, v176, v161, v162
	v_max3_f32 v176, v176, v163, v164
	v_max3_f32 v176, v176, v165, v166
	v_max3_f32 v176, v176, v167, v168
	v_max3_f32 v176, v176, v169, v170
	v_max_f32_e32 v176, v176, v171
	ds_write_b32 v179, v156 offset:59392
	ds_write_b32 v179, v157 offset:59648
	ds_write_b32 v179, v158 offset:59904
	ds_write_b32 v179, v159 offset:60160
	ds_write_b32 v179, v160 offset:60416
	ds_write_b32 v179, v161 offset:60672
	ds_write_b32 v179, v162 offset:60928
	ds_write_b32 v179, v163 offset:61184
	ds_write_b32 v179, v164 offset:61440
	ds_write_b32 v179, v165 offset:61696
	ds_write_b32 v179, v166 offset:61952
	ds_write_b32 v179, v167 offset:62208
	ds_write_b32 v179, v168 offset:62464
	ds_write_b32 v179, v169 offset:62720
	ds_write_b32 v179, v170 offset:62976
	ds_write_b32 v179, v171 offset:63232
	s_waitcnt lgkmcnt(0)
	global_load_dwordx4 v[140:143], v[172:173], off offset:512
	global_load_dwordx4 v[132:135], v[172:173], off offset:2560
	global_load_dwordx4 v[124:127], v[174:175], off offset:512
	global_load_dwordx4 v[116:119], v[174:175], off offset:2560
	v_mov_b32_e32 v156, v178
	v_mov_b32_e32 v157, v178
	v_mov_b32_e32 v158, v178
	v_mov_b32_e32 v159, v178
	v_mov_b32_e32 v160, v178
	v_mov_b32_e32 v161, v178
	v_mov_b32_e32 v162, v178
	v_mov_b32_e32 v163, v178
	v_mov_b32_e32 v164, v178
	v_mov_b32_e32 v165, v178
	v_mov_b32_e32 v166, v178
	v_mov_b32_e32 v167, v178
	v_mov_b32_e32 v168, v178
	v_mov_b32_e32 v169, v178
	v_mov_b32_e32 v170, v178
	v_mov_b32_e32 v171, v178
	s_waitcnt vmcnt(0)
	v_mfma_f32_32x32x16_f16 v[156:171], v[140:143], v[136:139], v[156:171]
	v_mfma_f32_32x32x16_f16 v[156:171], v[132:135], v[128:131], v[156:171]
	v_mfma_f32_32x32x16_f16 v[156:171], v[124:127], v[120:123], v[156:171]
	v_mfma_f32_32x32x16_f16 v[156:171], v[116:119], v[112:115], v[156:171]
	s_nop 15
	s_nop 3
	v_max3_f32 v177, v156, v157, v158
	v_max3_f32 v177, v177, v159, v160
	v_max3_f32 v177, v177, v161, v162
	v_max3_f32 v177, v177, v163, v164
	v_max3_f32 v177, v177, v165, v166
	v_max3_f32 v177, v177, v167, v168
	v_max3_f32 v177, v177, v169, v170
	v_max_f32_e32 v177, v177, v171
	v_max_f32_e32 v176, v176, v177
	v_mov_b32_e32 v177, v176
	s_nop 1
	v_permlane32_swap_b32_e32 v176, v177
	v_max_f32_e32 v176, v177, v176
	s_mov_b32 s37, 0x41000000
	v_cmp_lt_f32_e32 vcc, s37, v176
	v_max_f32_e32 v176, 0, v176
	s_nop 4
	s_cbranch_vccnz .Lmy_rare_2_rs
	v_mov_b32_e32 v176, 0
	s_branch .Lmy_rare_2_nr
.Lmy_rare_2_rs:
	v_add_f32_e32 v194, v194, v176
	v_exp_f32_e64 v177, -v176
	v_sub_f32_e32 v64, v64, v176
	v_sub_f32_e32 v65, v65, v176
	v_sub_f32_e32 v66, v66, v176
	v_sub_f32_e32 v67, v67, v176
	v_sub_f32_e32 v68, v68, v176
	v_sub_f32_e32 v69, v69, v176
	v_sub_f32_e32 v70, v70, v176
	v_sub_f32_e32 v71, v71, v176
	v_sub_f32_e32 v72, v72, v176
	v_sub_f32_e32 v73, v73, v176
	v_sub_f32_e32 v74, v74, v176
	v_sub_f32_e32 v75, v75, v176
	v_sub_f32_e32 v76, v76, v176
	v_sub_f32_e32 v77, v77, v176
	v_sub_f32_e32 v78, v78, v176
	v_sub_f32_e32 v79, v79, v176
	v_sub_f32_e32 v48, v48, v176
	v_sub_f32_e32 v49, v49, v176
	v_sub_f32_e32 v50, v50, v176
	v_sub_f32_e32 v51, v51, v176
	v_sub_f32_e32 v52, v52, v176
	v_sub_f32_e32 v53, v53, v176
	v_sub_f32_e32 v54, v54, v176
	v_sub_f32_e32 v55, v55, v176
	v_sub_f32_e32 v56, v56, v176
	v_sub_f32_e32 v57, v57, v176
	v_sub_f32_e32 v58, v58, v176
	v_sub_f32_e32 v59, v59, v176
	v_sub_f32_e32 v60, v60, v176
	v_sub_f32_e32 v61, v61, v176
	v_sub_f32_e32 v62, v62, v176
	v_sub_f32_e32 v63, v63, v176
	v_xor_b32_e32 v0, 0x80000000, v194
	v_mov_b32_e32 v1, v0
	v_mov_b32_e32 v2, v0
	v_mov_b32_e32 v3, v0
	v_mov_b32_e32 v4, v0
	v_mov_b32_e32 v5, v0
	v_mov_b32_e32 v6, v0
	v_mov_b32_e32 v7, v0
	v_mov_b32_e32 v8, v0
	v_mov_b32_e32 v9, v0
	v_mov_b32_e32 v10, v0
	v_mov_b32_e32 v11, v0
	v_mov_b32_e32 v12, v0
	v_mov_b32_e32 v13, v0
	v_mov_b32_e32 v14, v0
	v_mov_b32_e32 v15, v0
	v_mul_f32_e32 v187, v187, v177
	s_and_saveexec_b64 s[40:41], s[0:1]
	ds_write_b32 v186, v177 offset:57344
	s_or_b64 exec, exec, s[40:41]
	v_add_u32_e32 v178, s11, v193
	s_waitcnt lgkmcnt(0)
	ds_read_b128 v[140:143], v178 offset:57344
	ds_read_b128 v[132:135], v178 offset:57376
	ds_read_b128 v[124:127], v178 offset:57408
	ds_read_b128 v[116:119], v178 offset:57440
	s_waitcnt lgkmcnt(0)
	v_pk_mul_f32 v[16:17], v[16:17], v[140:141]
	v_pk_mul_f32 v[32:33], v[32:33], v[140:141]
	v_pk_mul_f32 v[18:19], v[18:19], v[142:143]
	v_pk_mul_f32 v[34:35], v[34:35], v[142:143]
	v_pk_mul_f32 v[20:21], v[20:21], v[132:133]
	v_pk_mul_f32 v[36:37], v[36:37], v[132:133]
	v_pk_mul_f32 v[22:23], v[22:23], v[134:135]
	v_pk_mul_f32 v[38:39], v[38:39], v[134:135]
	v_pk_mul_f32 v[24:25], v[24:25], v[124:125]
	v_pk_mul_f32 v[40:41], v[40:41], v[124:125]
	v_pk_mul_f32 v[26:27], v[26:27], v[126:127]
	v_pk_mul_f32 v[42:43], v[42:43], v[126:127]
	v_pk_mul_f32 v[28:29], v[28:29], v[116:117]
	v_pk_mul_f32 v[44:45], v[44:45], v[116:117]
	v_pk_mul_f32 v[30:31], v[30:31], v[118:119]
	v_pk_mul_f32 v[46:47], v[46:47], v[118:119]
.Lmy_rare_2_nr:
	v_sub_f32_e32 v156, v156, v176
	v_sub_f32_e32 v157, v157, v176
	v_sub_f32_e32 v158, v158, v176
	v_sub_f32_e32 v159, v159, v176
	v_sub_f32_e32 v160, v160, v176
	v_sub_f32_e32 v161, v161, v176
	v_sub_f32_e32 v162, v162, v176
	v_sub_f32_e32 v163, v163, v176
	v_sub_f32_e32 v164, v164, v176
	v_sub_f32_e32 v165, v165, v176
	v_sub_f32_e32 v166, v166, v176
	v_sub_f32_e32 v167, v167, v176
	v_sub_f32_e32 v168, v168, v176
	v_sub_f32_e32 v169, v169, v176
	v_sub_f32_e32 v170, v170, v176
	v_sub_f32_e32 v171, v171, v176
	v_exp_f32_e32 v156, v156
	v_exp_f32_e32 v157, v157
	v_exp_f32_e32 v158, v158
	v_exp_f32_e32 v159, v159
	v_exp_f32_e32 v160, v160
	v_exp_f32_e32 v161, v161
	v_exp_f32_e32 v162, v162
	v_exp_f32_e32 v163, v163
	v_exp_f32_e32 v164, v164
	v_exp_f32_e32 v165, v165
	v_exp_f32_e32 v166, v166
	v_exp_f32_e32 v167, v167
	v_exp_f32_e32 v168, v168
	v_exp_f32_e32 v169, v169
	v_exp_f32_e32 v170, v170
	v_exp_f32_e32 v171, v171
	s_nop 0
	v_add_f32_e32 v104, v156, v157
	v_add_f32_e32 v104, v158, v104
	v_add_f32_e32 v104, v159, v104
	v_add_f32_e32 v104, v160, v104
	v_add_f32_e32 v104, v161, v104
	v_add_f32_e32 v104, v162, v104
	v_add_f32_e32 v104, v163, v104
	v_add_f32_e32 v104, v164, v104
	v_add_f32_e32 v104, v165, v104
	v_add_f32_e32 v104, v166, v104
	v_add_f32_e32 v104, v167, v104
	v_add_f32_e32 v104, v168, v104
	v_add_f32_e32 v104, v169, v104
	v_add_f32_e32 v104, v170, v104
	v_add_f32_e32 v104, v171, v104
	v_cvt_pk_f16_f32 v124, v156, v157
	v_cvt_pk_f16_f32 v125, v158, v159
	v_cvt_pk_f16_f32 v126, v160, v161
	v_cvt_pk_f16_f32 v127, v162, v163
	v_cvt_pk_f16_f32 v116, v164, v165
	v_cvt_pk_f16_f32 v117, v166, v167
	v_cvt_pk_f16_f32 v118, v168, v169
	v_cvt_pk_f16_f32 v119, v170, v171
	ds_read_b32 v156, v179 offset:59392
	ds_read_b32 v157, v179 offset:59648
	ds_read_b32 v158, v179 offset:59904
	ds_read_b32 v159, v179 offset:60160
	ds_read_b32 v160, v179 offset:60416
	ds_read_b32 v161, v179 offset:60672
	ds_read_b32 v162, v179 offset:60928
	ds_read_b32 v163, v179 offset:61184
	ds_read_b32 v164, v179 offset:61440
	ds_read_b32 v165, v179 offset:61696
	ds_read_b32 v166, v179 offset:61952
	ds_read_b32 v167, v179 offset:62208
	ds_read_b32 v168, v179 offset:62464
	ds_read_b32 v169, v179 offset:62720
	ds_read_b32 v170, v179 offset:62976
	ds_read_b32 v171, v179 offset:63232
	s_waitcnt lgkmcnt(0)
	v_sub_f32_e32 v156, v156, v176
	v_sub_f32_e32 v157, v157, v176
	v_sub_f32_e32 v158, v158, v176
	v_sub_f32_e32 v159, v159, v176
	v_sub_f32_e32 v160, v160, v176
	v_sub_f32_e32 v161, v161, v176
	v_sub_f32_e32 v162, v162, v176
	v_sub_f32_e32 v163, v163, v176
	v_sub_f32_e32 v164, v164, v176
	v_sub_f32_e32 v165, v165, v176
	v_sub_f32_e32 v166, v166, v176
	v_sub_f32_e32 v167, v167, v176
	v_sub_f32_e32 v168, v168, v176
	v_sub_f32_e32 v169, v169, v176
	v_sub_f32_e32 v170, v170, v176
	v_sub_f32_e32 v171, v171, v176
	v_exp_f32_e32 v156, v156
	v_exp_f32_e32 v157, v157
	v_exp_f32_e32 v158, v158
	v_exp_f32_e32 v159, v159
	v_exp_f32_e32 v160, v160
	v_exp_f32_e32 v161, v161
	v_exp_f32_e32 v162, v162
	v_exp_f32_e32 v163, v163
	v_exp_f32_e32 v164, v164
	v_exp_f32_e32 v165, v165
	v_exp_f32_e32 v166, v166
	v_exp_f32_e32 v167, v167
	v_exp_f32_e32 v168, v168
	v_exp_f32_e32 v169, v169
	v_exp_f32_e32 v170, v170
	v_exp_f32_e32 v171, v171
	s_nop 0
	v_add_f32_e32 v104, v156, v104
	v_add_f32_e32 v104, v157, v104
	v_add_f32_e32 v104, v158, v104
	v_add_f32_e32 v104, v159, v104
	v_add_f32_e32 v104, v160, v104
	v_add_f32_e32 v104, v161, v104
	v_add_f32_e32 v104, v162, v104
	v_add_f32_e32 v104, v163, v104
	v_add_f32_e32 v104, v164, v104
	v_add_f32_e32 v104, v165, v104
	v_add_f32_e32 v104, v166, v104
	v_add_f32_e32 v104, v167, v104
	v_add_f32_e32 v104, v168, v104
	v_add_f32_e32 v104, v169, v104
	v_add_f32_e32 v104, v170, v104
	v_add_f32_e32 v104, v171, v104
	v_cvt_pk_f16_f32 v140, v156, v157
	v_cvt_pk_f16_f32 v141, v158, v159
	v_cvt_pk_f16_f32 v142, v160, v161
	v_cvt_pk_f16_f32 v143, v162, v163
	v_cvt_pk_f16_f32 v132, v164, v165
	v_cvt_pk_f16_f32 v133, v166, v167
	v_cvt_pk_f16_f32 v134, v168, v169
	v_cvt_pk_f16_f32 v135, v170, v171
	s_branch .Lmy_back_2

.Lmy_rare_3_rs:
	v_add_f32_e32 v194, v194, v164
	v_exp_f32_e64 v165, -v164
	v_sub_f32_e32 v80, v80, v164
	v_sub_f32_e32 v81, v81, v164
	v_sub_f32_e32 v82, v82, v164
	v_sub_f32_e32 v83, v83, v164
	v_sub_f32_e32 v84, v84, v164
	v_sub_f32_e32 v85, v85, v164
	v_sub_f32_e32 v86, v86, v164
	v_sub_f32_e32 v87, v87, v164
	v_sub_f32_e32 v88, v88, v164
	v_sub_f32_e32 v89, v89, v164
	v_sub_f32_e32 v90, v90, v164
	v_sub_f32_e32 v91, v91, v164
	v_sub_f32_e32 v92, v92, v164
	v_sub_f32_e32 v93, v93, v164
	v_sub_f32_e32 v94, v94, v164
	v_sub_f32_e32 v95, v95, v164
	v_sub_f32_e32 v0, v0, v164
	v_sub_f32_e32 v1, v1, v164
	v_sub_f32_e32 v2, v2, v164
	v_sub_f32_e32 v3, v3, v164
	v_sub_f32_e32 v4, v4, v164
	v_sub_f32_e32 v5, v5, v164
	v_sub_f32_e32 v6, v6, v164
	v_sub_f32_e32 v7, v7, v164
	v_sub_f32_e32 v8, v8, v164
	v_sub_f32_e32 v9, v9, v164
	v_sub_f32_e32 v10, v10, v164
	v_sub_f32_e32 v11, v11, v164
	v_sub_f32_e32 v12, v12, v164
	v_sub_f32_e32 v13, v13, v164
	v_sub_f32_e32 v14, v14, v164
	v_sub_f32_e32 v15, v15, v164
	v_mul_f32_e32 v187, v187, v165
	s_and_saveexec_b64 s[40:41], s[0:1]
	ds_write_b32 v186, v165 offset:57344
	s_or_b64 exec, exec, s[40:41]
	v_add_u32_e32 v166, s11, v193
	s_waitcnt lgkmcnt(0)
	ds_read_b128 v[140:143], v166 offset:57344
	ds_read_b128 v[132:135], v166 offset:57376
	ds_read_b128 v[124:127], v166 offset:57408
	ds_read_b128 v[116:119], v166 offset:57440
	s_waitcnt lgkmcnt(0)
	v_pk_mul_f32 v[16:17], v[16:17], v[140:141]
	v_pk_mul_f32 v[32:33], v[32:33], v[140:141]
	v_pk_mul_f32 v[18:19], v[18:19], v[142:143]
	v_pk_mul_f32 v[34:35], v[34:35], v[142:143]
	v_pk_mul_f32 v[20:21], v[20:21], v[132:133]
	v_pk_mul_f32 v[36:37], v[36:37], v[132:133]
	v_pk_mul_f32 v[22:23], v[22:23], v[134:135]
	v_pk_mul_f32 v[38:39], v[38:39], v[134:135]
	v_pk_mul_f32 v[24:25], v[24:25], v[124:125]
	v_pk_mul_f32 v[40:41], v[40:41], v[124:125]
	v_pk_mul_f32 v[26:27], v[26:27], v[126:127]
	v_pk_mul_f32 v[42:43], v[42:43], v[126:127]
	v_pk_mul_f32 v[28:29], v[28:29], v[116:117]
	v_pk_mul_f32 v[44:45], v[44:45], v[116:117]
	v_pk_mul_f32 v[30:31], v[30:31], v[118:119]
	v_pk_mul_f32 v[46:47], v[46:47], v[118:119]
.Lmy_rare_3_nr:
	v_sub_f32_e32 v144, v144, v164
	v_sub_f32_e32 v145, v145, v164
	v_sub_f32_e32 v146, v146, v164
	v_sub_f32_e32 v147, v147, v164
	v_sub_f32_e32 v148, v148, v164
	v_sub_f32_e32 v149, v149, v164
	v_sub_f32_e32 v150, v150, v164
	v_sub_f32_e32 v151, v151, v164
	v_sub_f32_e32 v152, v152, v164
	v_sub_f32_e32 v153, v153, v164
	v_sub_f32_e32 v154, v154, v164
	v_sub_f32_e32 v155, v155, v164
	v_sub_f32_e32 v156, v156, v164
	v_sub_f32_e32 v157, v157, v164
	v_sub_f32_e32 v158, v158, v164
	v_sub_f32_e32 v159, v159, v164
	v_exp_f32_e32 v144, v144
	v_exp_f32_e32 v145, v145
	v_exp_f32_e32 v146, v146
	v_exp_f32_e32 v147, v147
	v_exp_f32_e32 v148, v148
	v_exp_f32_e32 v149, v149
	v_exp_f32_e32 v150, v150
	v_exp_f32_e32 v151, v151
	v_exp_f32_e32 v152, v152
	v_exp_f32_e32 v153, v153
	v_exp_f32_e32 v154, v154
	v_exp_f32_e32 v155, v155
	v_exp_f32_e32 v156, v156
	v_exp_f32_e32 v157, v157
	v_exp_f32_e32 v158, v158
	v_exp_f32_e32 v159, v159
	s_nop 0
	v_add_f32_e32 v48, v144, v145
	v_add_f32_e32 v48, v146, v48
	v_add_f32_e32 v48, v147, v48
	v_add_f32_e32 v48, v148, v48
	v_add_f32_e32 v48, v149, v48
	v_add_f32_e32 v48, v150, v48
	v_add_f32_e32 v48, v151, v48
	v_add_f32_e32 v48, v152, v48
	v_add_f32_e32 v48, v153, v48
	v_add_f32_e32 v48, v154, v48
	v_add_f32_e32 v48, v155, v48
	v_add_f32_e32 v48, v156, v48
	v_add_f32_e32 v48, v157, v48
	v_add_f32_e32 v48, v158, v48
	v_add_f32_e32 v48, v159, v48
	v_cvt_pk_f16_f32 v124, v144, v145
	v_cvt_pk_f16_f32 v125, v146, v147
	v_cvt_pk_f16_f32 v126, v148, v149
	v_cvt_pk_f16_f32 v127, v150, v151
	v_cvt_pk_f16_f32 v116, v152, v153
	v_cvt_pk_f16_f32 v117, v154, v155
	v_cvt_pk_f16_f32 v118, v156, v157
	v_cvt_pk_f16_f32 v119, v158, v159
	ds_read_b32 v144, v167 offset:59392
	ds_read_b32 v145, v167 offset:59648
	ds_read_b32 v146, v167 offset:59904
	ds_read_b32 v147, v167 offset:60160
	ds_read_b32 v148, v167 offset:60416
	ds_read_b32 v149, v167 offset:60672
	ds_read_b32 v150, v167 offset:60928
	ds_read_b32 v151, v167 offset:61184
	ds_read_b32 v152, v167 offset:61440
	ds_read_b32 v153, v167 offset:61696
	ds_read_b32 v154, v167 offset:61952
	ds_read_b32 v155, v167 offset:62208
	ds_read_b32 v156, v167 offset:62464
	ds_read_b32 v157, v167 offset:62720
	ds_read_b32 v158, v167 offset:62976
	ds_read_b32 v159, v167 offset:63232
	s_waitcnt lgkmcnt(0)
	v_sub_f32_e32 v144, v144, v164
	v_sub_f32_e32 v145, v145, v164
	v_sub_f32_e32 v146, v146, v164
	v_sub_f32_e32 v147, v147, v164
	v_sub_f32_e32 v148, v148, v164
	v_sub_f32_e32 v149, v149, v164
	v_sub_f32_e32 v150, v150, v164
	v_sub_f32_e32 v151, v151, v164
	v_sub_f32_e32 v152, v152, v164
	v_sub_f32_e32 v153, v153, v164
	v_sub_f32_e32 v154, v154, v164
	v_sub_f32_e32 v155, v155, v164
	v_sub_f32_e32 v156, v156, v164
	v_sub_f32_e32 v157, v157, v164
	v_sub_f32_e32 v158, v158, v164
	v_sub_f32_e32 v159, v159, v164
	v_exp_f32_e32 v144, v144
	v_exp_f32_e32 v145, v145
	v_exp_f32_e32 v146, v146
	v_exp_f32_e32 v147, v147
	v_exp_f32_e32 v148, v148
	v_exp_f32_e32 v149, v149
	v_exp_f32_e32 v150, v150
	v_exp_f32_e32 v151, v151
	v_exp_f32_e32 v152, v152
	v_exp_f32_e32 v153, v153
	v_exp_f32_e32 v154, v154
	v_exp_f32_e32 v155, v155
	v_exp_f32_e32 v156, v156
	v_exp_f32_e32 v157, v157
	v_exp_f32_e32 v158, v158
	v_exp_f32_e32 v159, v159
	s_nop 0
	v_add_f32_e32 v48, v144, v48
	v_add_f32_e32 v48, v145, v48
	v_add_f32_e32 v48, v146, v48
	v_add_f32_e32 v48, v147, v48
	v_add_f32_e32 v48, v148, v48
	v_add_f32_e32 v48, v149, v48
	v_add_f32_e32 v48, v150, v48
	v_add_f32_e32 v48, v151, v48
	v_add_f32_e32 v48, v152, v48
	v_add_f32_e32 v48, v153, v48
	v_add_f32_e32 v48, v154, v48
	v_add_f32_e32 v48, v155, v48
	v_add_f32_e32 v48, v156, v48
	v_add_f32_e32 v48, v157, v48
	v_add_f32_e32 v48, v158, v48
	v_add_f32_e32 v48, v159, v48
	v_cvt_pk_f16_f32 v140, v144, v145
	v_cvt_pk_f16_f32 v141, v146, v147
	v_cvt_pk_f16_f32 v142, v148, v149
	v_cvt_pk_f16_f32 v143, v150, v151
	v_cvt_pk_f16_f32 v132, v152, v153
	v_cvt_pk_f16_f32 v133, v154, v155
	v_cvt_pk_f16_f32 v134, v156, v157
	v_cvt_pk_f16_f32 v135, v158, v159
	s_branch .Lmy_back_3
.Lmy_rare_4:
	v_subrev_u32_e32 v160, s25, v191
	v_ashrrev_i32_e32 v161, 31, v160
	v_lshl_add_u64 v[160:161], v[182:183], 0, v[160:161]
	s_mov_b64 s[38:39], 0x1000
	v_lshl_add_u64 v[162:163], v[160:161], 0, s[38:39]
	v_xor_b32_e32 v166, 0x80000000, v194
	s_lshl_b32 s42, s23, 12
	v_lshlrev_b32_e32 v167, 2, v188
	v_add_u32_e32 v167, s42, v167
	global_load_dwordx4 v[140:143], v[160:161], off
	global_load_dwordx4 v[132:135], v[160:161], off offset:2048
	global_load_dwordx4 v[124:127], v[162:163], off
	global_load_dwordx4 v[116:119], v[162:163], off offset:2048
	v_mov_b32_e32 v144, v166
	v_mov_b32_e32 v145, v166
	v_mov_b32_e32 v146, v166
	v_mov_b32_e32 v147, v166
	v_mov_b32_e32 v148, v166
	v_mov_b32_e32 v149, v166
	v_mov_b32_e32 v150, v166
	v_mov_b32_e32 v151, v166
	v_mov_b32_e32 v152, v166
	v_mov_b32_e32 v153, v166
	v_mov_b32_e32 v154, v166
	v_mov_b32_e32 v155, v166
	v_mov_b32_e32 v156, v166
	v_mov_b32_e32 v157, v166
	v_mov_b32_e32 v158, v166
	v_mov_b32_e32 v159, v166
	s_waitcnt vmcnt(0)
	v_mfma_f32_32x32x16_f16 v[144:159], v[140:143], v[136:139], v[144:159]
	v_mfma_f32_32x32x16_f16 v[144:159], v[132:135], v[128:131], v[144:159]
	v_mfma_f32_32x32x16_f16 v[144:159], v[124:127], v[120:123], v[144:159]
	v_mfma_f32_32x32x16_f16 v[144:159], v[116:119], v[112:115], v[144:159]
	s_nop 15
	s_nop 3
	v_max3_f32 v164, v144, v145, v146
	v_max3_f32 v164, v164, v147, v148
	v_max3_f32 v164, v164, v149, v150
	v_max3_f32 v164, v164, v151, v152
	v_max3_f32 v164, v164, v153, v154
	v_max3_f32 v164, v164, v155, v156
	v_max3_f32 v164, v164, v157, v158
	v_max_f32_e32 v164, v164, v159
	ds_write_b32 v167, v144 offset:59392
	ds_write_b32 v167, v145 offset:59648
	ds_write_b32 v167, v146 offset:59904
	ds_write_b32 v167, v147 offset:60160
	ds_write_b32 v167, v148 offset:60416
	ds_write_b32 v167, v149 offset:60672
	ds_write_b32 v167, v150 offset:60928
	ds_write_b32 v167, v151 offset:61184
	ds_write_b32 v167, v152 offset:61440
	ds_write_b32 v167, v153 offset:61696
	ds_write_b32 v167, v154 offset:61952
	ds_write_b32 v167, v155 offset:62208
	ds_write_b32 v167, v156 offset:62464
	ds_write_b32 v167, v157 offset:62720
	ds_write_b32 v167, v158 offset:62976
	ds_write_b32 v167, v159 offset:63232
	s_waitcnt lgkmcnt(0)
	global_load_dwordx4 v[140:143], v[160:161], off offset:512
	global_load_dwordx4 v[132:135], v[160:161], off offset:2560
	global_load_dwordx4 v[124:127], v[162:163], off offset:512
	global_load_dwordx4 v[116:119], v[162:163], off offset:2560
	v_mov_b32_e32 v144, v166
	v_mov_b32_e32 v145, v166
	v_mov_b32_e32 v146, v166
	v_mov_b32_e32 v147, v166
	v_mov_b32_e32 v148, v166
	v_mov_b32_e32 v149, v166
	v_mov_b32_e32 v150, v166
	v_mov_b32_e32 v151, v166
	v_mov_b32_e32 v152, v166
	v_mov_b32_e32 v153, v166
	v_mov_b32_e32 v154, v166
	v_mov_b32_e32 v155, v166
	v_mov_b32_e32 v156, v166
	v_mov_b32_e32 v157, v166
	v_mov_b32_e32 v158, v166
	v_mov_b32_e32 v159, v166
	s_waitcnt vmcnt(0)
	v_mfma_f32_32x32x16_f16 v[144:159], v[140:143], v[136:139], v[144:159]
	v_mfma_f32_32x32x16_f16 v[144:159], v[132:135], v[128:131], v[144:159]
	v_mfma_f32_32x32x16_f16 v[144:159], v[124:127], v[120:123], v[144:159]
	v_mfma_f32_32x32x16_f16 v[144:159], v[116:119], v[112:115], v[144:159]
	s_nop 15
	s_nop 3
	v_max3_f32 v165, v144, v145, v146
	v_max3_f32 v165, v165, v147, v148
	v_max3_f32 v165, v165, v149, v150
	v_max3_f32 v165, v165, v151, v152
	v_max3_f32 v165, v165, v153, v154
	v_max3_f32 v165, v165, v155, v156
	v_max3_f32 v165, v165, v157, v158
	v_max_f32_e32 v165, v165, v159
	v_max_f32_e32 v164, v164, v165
	v_mov_b32_e32 v165, v164
	s_nop 1
	v_permlane32_swap_b32_e32 v164, v165
	v_max_f32_e32 v164, v165, v164
	s_mov_b32 s37, 0x41000000
	v_cmp_lt_f32_e32 vcc, s37, v164
	v_max_f32_e32 v164, 0, v164
	s_nop 4
	s_cbranch_vccnz .Lmy_rare_4_rs
	v_mov_b32_e32 v164, 0
	s_branch .Lmy_rare_4_nr
.Lmy_rare_4_rs:
	v_add_f32_e32 v194, v194, v164
	v_exp_f32_e64 v165, -v164
	s_nop 0
	v_mul_f32_e32 v197, v197, v165
	s_and_saveexec_b64 s[40:41], s[0:1]
	ds_write_b32 v186, v165 offset:57344
	s_or_b64 exec, exec, s[40:41]
	v_add_u32_e32 v166, s11, v193
	s_waitcnt lgkmcnt(0)
	ds_read_b128 v[140:143], v166 offset:57344
	ds_read_b128 v[132:135], v166 offset:57376
	ds_read_b128 v[124:127], v166 offset:57408
	ds_read_b128 v[116:119], v166 offset:57440
	s_waitcnt lgkmcnt(0)
	v_pk_mul_f32 v[16:17], v[16:17], v[140:141]
	v_pk_mul_f32 v[32:33], v[32:33], v[140:141]
	v_pk_mul_f32 v[18:19], v[18:19], v[142:143]
	v_pk_mul_f32 v[34:35], v[34:35], v[142:143]
	v_pk_mul_f32 v[20:21], v[20:21], v[132:133]
	v_pk_mul_f32 v[36:37], v[36:37], v[132:133]
	v_pk_mul_f32 v[22:23], v[22:23], v[134:135]
	v_pk_mul_f32 v[38:39], v[38:39], v[134:135]
	v_pk_mul_f32 v[24:25], v[24:25], v[124:125]
	v_pk_mul_f32 v[40:41], v[40:41], v[124:125]
	v_pk_mul_f32 v[26:27], v[26:27], v[126:127]
	v_pk_mul_f32 v[42:43], v[42:43], v[126:127]
	v_pk_mul_f32 v[28:29], v[28:29], v[116:117]
	v_pk_mul_f32 v[44:45], v[44:45], v[116:117]
	v_pk_mul_f32 v[30:31], v[30:31], v[118:119]
	v_pk_mul_f32 v[46:47], v[46:47], v[118:119]
.Lmy_rare_4_nr:
	v_sub_f32_e32 v144, v144, v164
	v_sub_f32_e32 v145, v145, v164
	v_sub_f32_e32 v146, v146, v164
	v_sub_f32_e32 v147, v147, v164
	v_sub_f32_e32 v148, v148, v164
	v_sub_f32_e32 v149, v149, v164
	v_sub_f32_e32 v150, v150, v164
	v_sub_f32_e32 v151, v151, v164
	v_sub_f32_e32 v152, v152, v164
	v_sub_f32_e32 v153, v153, v164
	v_sub_f32_e32 v154, v154, v164
	v_sub_f32_e32 v155, v155, v164
	v_sub_f32_e32 v156, v156, v164
	v_sub_f32_e32 v157, v157, v164
	v_sub_f32_e32 v158, v158, v164
	v_sub_f32_e32 v159, v159, v164
	v_exp_f32_e32 v0, v144
	v_exp_f32_e32 v1, v145
	v_exp_f32_e32 v2, v146
	v_exp_f32_e32 v3, v147
	v_exp_f32_e32 v4, v148
	v_exp_f32_e32 v5, v149
	v_exp_f32_e32 v6, v150
	v_exp_f32_e32 v7, v151
	v_exp_f32_e32 v8, v152
	v_exp_f32_e32 v9, v153
	v_exp_f32_e32 v10, v154
	v_exp_f32_e32 v11, v155
	v_exp_f32_e32 v12, v156
	v_exp_f32_e32 v13, v157
	v_exp_f32_e32 v14, v158
	v_exp_f32_e32 v15, v159
	ds_read_b32 v144, v167 offset:59392
	ds_read_b32 v145, v167 offset:59648
	ds_read_b32 v146, v167 offset:59904
	ds_read_b32 v147, v167 offset:60160
	ds_read_b32 v148, v167 offset:60416
	ds_read_b32 v149, v167 offset:60672
	ds_read_b32 v150, v167 offset:60928
	ds_read_b32 v151, v167 offset:61184
	ds_read_b32 v152, v167 offset:61440
	ds_read_b32 v153, v167 offset:61696
	ds_read_b32 v154, v167 offset:61952
	ds_read_b32 v155, v167 offset:62208
	ds_read_b32 v156, v167 offset:62464
	ds_read_b32 v157, v167 offset:62720
	ds_read_b32 v158, v167 offset:62976
	ds_read_b32 v159, v167 offset:63232
	s_waitcnt lgkmcnt(0)
	v_sub_f32_e32 v144, v144, v164
	v_sub_f32_e32 v145, v145, v164
	v_sub_f32_e32 v146, v146, v164
	v_sub_f32_e32 v147, v147, v164
	v_sub_f32_e32 v148, v148, v164
	v_sub_f32_e32 v149, v149, v164
	v_sub_f32_e32 v150, v150, v164
	v_sub_f32_e32 v151, v151, v164
	v_sub_f32_e32 v152, v152, v164
	v_sub_f32_e32 v153, v153, v164
	v_sub_f32_e32 v154, v154, v164
	v_sub_f32_e32 v155, v155, v164
	v_sub_f32_e32 v156, v156, v164
	v_sub_f32_e32 v157, v157, v164
	v_sub_f32_e32 v158, v158, v164
	v_sub_f32_e32 v159, v159, v164
	v_exp_f32_e32 v80, v144
	v_exp_f32_e32 v81, v145
	v_exp_f32_e32 v82, v146
	v_exp_f32_e32 v83, v147
	v_exp_f32_e32 v84, v148
	v_exp_f32_e32 v85, v149
	v_exp_f32_e32 v86, v150
	v_exp_f32_e32 v87, v151
	v_exp_f32_e32 v88, v152
	v_exp_f32_e32 v89, v153
	v_exp_f32_e32 v90, v154
	v_exp_f32_e32 v91, v155
	v_exp_f32_e32 v92, v156
	v_exp_f32_e32 v93, v157
	v_exp_f32_e32 v94, v158
	v_exp_f32_e32 v95, v159
	s_branch .Lmy_back_4

	.amdhsa_kernel _Z11attn_kernelPKDF16_S0_PDF16_
		.amdhsa_group_segment_fixed_size 0
		.amdhsa_private_segment_fixed_size 0
		.amdhsa_kernarg_size 24
		.amdhsa_user_sgpr_count 2
		.amdhsa_user_sgpr_dispatch_ptr 0
		.amdhsa_user_sgpr_queue_ptr 0
		.amdhsa_user_sgpr_kernarg_segment_ptr 1
		.amdhsa_user_sgpr_dispatch_id 0
		.amdhsa_user_sgpr_kernarg_preload_length 0
		.amdhsa_user_sgpr_kernarg_preload_offset 0
		.amdhsa_user_sgpr_private_segment_size 0
		.amdhsa_uses_dynamic_stack 0
		.amdhsa_enable_private_segment 0
		.amdhsa_system_sgpr_workgroup_id_x 1
		.amdhsa_system_sgpr_workgroup_id_y 0
		.amdhsa_system_sgpr_workgroup_id_z 0
		.amdhsa_system_sgpr_workgroup_info 0
		.amdhsa_system_vgpr_workitem_id 0
		.amdhsa_next_free_vgpr 199
		.amdhsa_next_free_sgpr 43
		.amdhsa_accum_offset 200
		.amdhsa_reserve_vcc 1
		.amdhsa_float_round_mode_32 0
		.amdhsa_float_round_mode_16_64 0
		.amdhsa_float_denorm_mode_32 3
		.amdhsa_float_denorm_mode_16_64 3
		.amdhsa_dx10_clamp 1
		.amdhsa_ieee_mode 1
		.amdhsa_fp16_overflow 0
		.amdhsa_tg_split 0
		.amdhsa_exception_fp_ieee_invalid_op 0
		.amdhsa_exception_fp_denorm_src 0
		.amdhsa_exception_fp_ieee_div_zero 0
		.amdhsa_exception_fp_ieee_overflow 0
		.amdhsa_exception_fp_ieee_underflow 0
		.amdhsa_exception_fp_ieee_inexact 0
		.amdhsa_exception_int_div_zero 0
	.end_amdhsa_kernel

amdhsa.kernels:
  - .agpr_count:     0
    .args:
      - .actual_access:  read_only
        .address_space:  global
        .offset:         0
        .size:           8
        .value_kind:     global_buffer
      - .actual_access:  read_only
        .address_space:  global
        .offset:         8
        .size:           8
        .value_kind:     global_buffer
      - .actual_access:  read_only
        .address_space:  global
        .offset:         16
        .size:           8
        .value_kind:     global_buffer
      - .actual_access:  read_only
        .address_space:  global
        .offset:         24
        .size:           8
        .value_kind:     global_buffer
      - .actual_access:  read_only
        .address_space:  global
        .offset:         32
        .size:           8
        .value_kind:     global_buffer
      - .actual_access:  write_only
        .address_space:  global
        .offset:         40
        .size:           8
        .value_kind:     global_buffer
      - .actual_access:  write_only
        .address_space:  global
        .offset:         48
        .size:           8
        .value_kind:     global_buffer
      - .actual_access:  write_only
        .address_space:  global
        .offset:         56
        .size:           8
        .value_kind:     global_buffer
      - .actual_access:  write_only
        .address_space:  global
        .offset:         64
        .size:           8
        .value_kind:     global_buffer
    .group_segment_fixed_size: 0
    .kernarg_segment_align: 8
    .kernarg_segment_size: 72
    .language:       OpenCL C
    .language_version:
      - 2
      - 0
    .max_flat_workgroup_size: 256
    .name:           _Z11prep_kernelPKfS0_S0_S0_S0_PDF16_S1_S1_S1_
    .private_segment_fixed_size: 0
    .sgpr_count:     21
    .sgpr_spill_count: 0
    .symbol:         _Z11prep_kernelPKfS0_S0_S0_S0_PDF16_S1_S1_S1_.kd
    .uniform_work_group_size: 1
    .uses_dynamic_stack: false
    .vgpr_count:     18
    .vgpr_spill_count: 0
    .wavefront_size: 64
  - .agpr_count:     0
    .args:
      - .actual_access:  read_only
        .address_space:  global
        .offset:         0
        .size:           8
        .value_kind:     global_buffer
      - .actual_access:  read_only
        .address_space:  global
        .offset:         8
        .size:           8
        .value_kind:     global_buffer
      - .actual_access:  read_only
        .address_space:  global
        .offset:         16
        .size:           8
        .value_kind:     global_buffer
      - .actual_access:  read_only
        .address_space:  global
        .offset:         24
        .size:           8
        .value_kind:     global_buffer
      - .actual_access:  read_only
        .address_space:  global
        .offset:         32
        .size:           8
        .value_kind:     global_buffer
      - .actual_access:  write_only
        .address_space:  global
        .offset:         40
        .size:           8
        .value_kind:     global_buffer
      - .actual_access:  write_only
        .address_space:  global
        .offset:         48
        .size:           8
        .value_kind:     global_buffer
    .group_segment_fixed_size: 0
    .kernarg_segment_align: 8
    .kernarg_segment_size: 56
    .language:       OpenCL C
    .language_version:
      - 2
      - 0
    .max_flat_workgroup_size: 512
    .name:           _Z11proj_kernelPKfS0_PKDF16_S0_S0_PDF16_S3_
    .private_segment_fixed_size: 0
    .sgpr_count:     21
    .sgpr_spill_count: 0
    .symbol:         _Z11proj_kernelPKfS0_PKDF16_S0_S0_PDF16_S3_.kd
    .uniform_work_group_size: 1
    .uses_dynamic_stack: false
    .vgpr_count:     170
    .vgpr_spill_count: 0
    .wavefront_size: 64
  - .agpr_count:     0
    .args:
      - .address_space:  global
        .offset:         0
        .size:           8
        .value_kind:     global_buffer
      - .address_space:  global
        .offset:         8
        .size:           8
        .value_kind:     global_buffer
      - .actual_access:  write_only
        .address_space:  global
        .offset:         16
        .size:           8
        .value_kind:     global_buffer
    .group_segment_fixed_size: 0
    .kernarg_segment_align: 8
    .kernarg_segment_size: 24
    .language:       OpenCL C
    .language_version:
      - 2
      - 0
    .max_flat_workgroup_size: 512
    .name:           _Z11attn_kernelPKDF16_S0_PDF16_
    .private_segment_fixed_size: 0
    .sgpr_count:     49
    .sgpr_spill_count: 0
    .symbol:         _Z11attn_kernelPKDF16_S0_PDF16_.kd
    .uniform_work_group_size: 1
    .uses_dynamic_stack: false
    .vgpr_count:     199
    .vgpr_spill_count: 0
    .wavefront_size: 64
  - .agpr_count:     0
    .args:
      - .actual_access:  read_only
        .address_space:  global
        .offset:         0
        .size:           8
        .value_kind:     global_buffer
      - .actual_access:  read_only
        .address_space:  global
        .offset:         8
        .size:           8
        .value_kind:     global_buffer
      - .actual_access:  read_only
        .address_space:  global
        .offset:         16
        .size:           8
        .value_kind:     global_buffer
      - .actual_access:  read_only
        .address_space:  global
        .offset:         24
        .size:           8
        .value_kind:     global_buffer
      - .actual_access:  read_only
        .address_space:  global
        .offset:         32
        .size:           8
        .value_kind:     global_buffer
      - .address_space:  global
        .offset:         40
        .size:           8
        .value_kind:     global_buffer
      - .actual_access:  read_only
        .address_space:  global
        .offset:         48
        .size:           8
        .value_kind:     global_buffer
      - .actual_access:  read_only
        .address_space:  global
        .offset:         56
        .size:           8
        .value_kind:     global_buffer
      - .actual_access:  read_only
        .address_space:  global
        .offset:         64
        .size:           8
        .value_kind:     global_buffer
      - .address_space:  global
        .offset:         72
        .size:           8
        .value_kind:     global_buffer
      - .actual_access:  read_only
        .address_space:  global
        .offset:         80
        .size:           8
        .value_kind:     global_buffer
      - .actual_access:  write_only
        .address_space:  global
        .offset:         88
        .size:           8
        .value_kind:     global_buffer
    .group_segment_fixed_size: 0
    .kernarg_segment_align: 8
    .kernarg_segment_size: 96
    .language:       OpenCL C
    .language_version:
      - 2
      - 0
    .max_flat_workgroup_size: 512
    .name:           _Z10ffn_kernelPKfS0_PKDF16_S2_S0_S2_S0_S0_S0_S2_S0_Pf
    .private_segment_fixed_size: 0
    .sgpr_count:     24
    .sgpr_spill_count: 0
    .symbol:         _Z10ffn_kernelPKfS0_PKDF16_S2_S0_S2_S0_S0_S0_S2_S0_Pf.kd
    .uniform_work_group_size: 1
    .uses_dynamic_stack: false
    .vgpr_count:     230
    .vgpr_spill_count: 0
    .wavefront_size: 64
